# P0 rebalancing variant: GEMV workgroups take 1 conversion item per wave, ids 0-95 a second one (1.5 on average)
# baseline (speedup 1.0000x reference)
.LBB0_41:
	s_or_b64 exec, exec, s[2:3]
	s_lshl_b32 s2, s80, 3
	s_add_i32 s16, s97, s2
	s_lshl_b32 s17, s62, 3
	s_movk_i32 s32, 0x2020
	s_cmpk_lg_i32 s62, 0x100
	s_cbranch_scc1 .Lp0_go
	s_cmpk_lt_u32 s80, 0xc0
	s_cbranch_scc0 .Lp0_tbl
	s_movk_i32 s17, 0x600
	s_movk_i32 s32, 0x600
	s_cmpk_lt_u32 s80, 0x60
	s_cbranch_scc0 .Lp0_go
	s_movk_i32 s32, 0x900
	s_branch .Lp0_go
.Lp0_tbl:
	s_addk_i32 s16, 0x300
	s_movk_i32 s17, 0x200
